# attention mask LUT re-laid out at index 17*hi+lo (bank group hi+lo instead of lo) to spread LDS bank conflicts; address = (byte*17)&-16, two VALU per byte
# speedup vs baseline: 1.0066x; 1.0066x over previous
; __device__ __forceinline__ int crow(int r, int hi) { return (r & 3) + 8 * (r >> 2) + 4 * hi; }
; __device__ __forceinline__ int crow(int r,int hi){return (r&3)+8*(r>>2)+4*hi;}
; #define REP(n) for (int rep_ = 0; rep_ < 1 + MK_REPN * (((MK_DUP) >> (n)) & 1); ++rep_)
; template<int THRL> __device__ __forceinline__ void attn_unit(int b,int h,int qb,const bf16*Q,const bf16*__restrict__ K,const bf16*__restrict__ V,bf16*O,const unsigned*MASK,char*shm){
;     ...
;   {auto rr=__builtin_amdgcn_permlane32_swap(__float_as_uint(l_reg),__float_as_uint(l_reg),false,false);l_reg=__uint_as_float(rr[0])+__uint_as_float(rr[1]);}
;   if(hi==0)wsf[32+r32]=l_reg;asm volatile("s_waitcnt lgkmcnt(0)":::"memory");
;   float rli[16];
;   #pragma unroll
;   for(int r=0;r<16;++r)rli[r]=__builtin_amdgcn_rcpf(wsf[32+crow(r,hi)]);
;   bf16*Ow=O+(rowbase+q0+wid*QBLK)*OPITCH+h*D;
;   { bf16*stg=(bf16*)(shm+LDS_OST)+wid*2048;
;     #pragma unroll
;     for(int r=0;r<16;++r){const int orow=crow(r,hi);
;       #pragma unroll
;       for(int d0=0;d0<2;++d0)stg[orow*64+d0*32+r32]=__float2bfloat16(o[d0][r]*rli[r]);}
;     asm volatile("s_waitcnt lgkmcnt(0)":::"memory");
;     #pragma unroll
;     for(int i=0;i<4;++i){const int row=i*8+(lane>>3),ch=lane&7; const u32x4 v=*(const u32x4*)(stg+row*64+ch*8); ATTN_STORE16(Ow+(long)row*OPITCH+ch*8,v);} }
;   asm volatile("s_waitcnt lgkmcnt(0)\n\ts_barrier":::"memory");
; __global__ void __launch_bounds__(NWAVES * 64, 2) mk_fwd(Args args) {
;     ...
;             { const attn_body::AttnTensors AT{(const attn_body::bf16*)(ws + WS_Q), (const attn_body::bf16*)(ws + WS_K), (const attn_body::bf16*)(ws + WS_V), (attn_body::bf16*)(ws + WS_MIX) + 512, (const unsigned*)(ws + (l ? WS_MASK1 : WS_MASK))};
;               const attn_body::StaticOrder S((int)F.G, (int)blockIdx.x);
;               REP(6) attn_body::attn_phase<attn_body::StaticOrder>((char*)lds + RING_OFF, AT, S); }
.LBB0_1258:
	s_andn2_b64 vcc, exec, s[4:5]
	s_cbranch_vccnz .LBB0_1395
	v_mov_b32_e32 v204, 0x3f803f80
	v_mov_b32_e32 v205, 0x3f803f80
	v_mov_b32_e32 v206, 0x3f803f80
	v_mov_b32_e32 v207, 0x3f803f80
	s_mov_b32 s32, 17
	v_lshrrev_b32_e32 v228, 1, v0
	v_and_b32_e32 v229, 1, v0
	v_lshlrev_b32_e32 v230, 2, v229
	v_lshrrev_b32_e32 v231, v230, v228
	v_bfe_i32 v232, v231, 0, 1
	v_bfe_i32 v233, v231, 1, 1
	v_and_b32_e32 v232, 0xffff, v232
	v_and_b32_e32 v233, 0xffff0000, v233
	v_or_b32_e32 v232, v232, v233
	v_bfe_i32 v233, v231, 2, 1
	v_bfe_i32 v234, v231, 3, 1
	v_and_b32_e32 v233, 0xffff, v233
	v_and_b32_e32 v234, 0xffff0000, v234
	v_or_b32_e32 v233, v233, v234
	v_mul_u32_u24_e32 v234, 17, v228
	v_and_b32_e32 v234, -16, v234
	v_lshl_add_u32 v234, v229, 3, v234
	ds_write_b64 v234, v[232:233] offset:51200
	v_mov_b32_e32 v1, v0
	s_mov_b64 s[4:5], s[66:67]
	s_load_dwordx2 s[4:5], s[4:5], 0xd0
	v_readlane_b32 s6, v252, 16
	v_readlane_b32 s7, v252, 17
	s_mov_b32 s55, 0
	s_waitcnt lgkmcnt(0)
	s_add_u32 s8, s4, 0xea00000
	s_addc_u32 s9, s5, 0
	s_add_u32 s17, s4, 0x10a00000
	s_addc_u32 s18, s5, 0
	s_add_u32 s19, s4, 0x12a00000
	s_addc_u32 s20, s5, 0
	s_add_u32 s21, s4, 0x15f00400
	s_addc_u32 s22, s5, 0
	s_add_u32 s23, s4, s6
	s_addc_u32 s54, s5, s7
	s_branch .LBB0_1262
.LBB0_1260:
	s_or_b64 exec, exec, s[4:5]
	s_waitcnt lgkmcnt(0)
	ds_read_b128 v[36:39], v52 offset:49280
	ds_read_b128 v[40:43], v52 offset:49312
	s_lshl_b64 s[4:5], s[44:45], 11
	s_add_u32 s4, s21, s4
	s_addc_u32 s5, s22, s5
	s_waitcnt lgkmcnt(1)
	v_rcp_f32_e32 v2, v228
	v_rcp_f32_e32 v44, v229
	s_lshl_b32 s7, s7, 12
	v_rcp_f32_e32 v45, v230
	v_rcp_f32_e32 v46, v231
	s_waitcnt lgkmcnt(0)
	v_rcp_f32_e32 v47, v232
	ds_read_b128 v[36:39], v52 offset:49344
	v_rcp_f32_e32 v48, v233
	v_rcp_f32_e32 v49, v234
	v_rcp_f32_e32 v50, v235
	ds_read_b128 v[40:43], v52 offset:49376
	s_add_i32 s7, s7, 0
	v_lshlrev_b32_e32 v51, 9, v214
	v_lshlrev_b32_e32 v52, 1, v213
	v_mul_f32_e32 v20, v20, v2
	v_mul_f32_e32 v2, v4, v2
	v_add3_u32 v51, s7, v51, v52
	v_cvt_pk_bf16_f32 v2, v2, s0
	ds_write_b16 v51, v2 offset:55616
	v_mul_f32_e32 v2, v21, v44
	v_cvt_pk_bf16_f32 v2, v2, s0
	ds_write_b16 v51, v2 offset:55680
	v_mul_f32_e32 v2, v5, v44
	v_cvt_pk_bf16_f32 v2, v2, s0
	ds_write_b16 v51, v2 offset:55744
	v_mul_f32_e32 v2, v22, v45
	v_cvt_pk_bf16_f32 v2, v2, s0
	ds_write_b16 v51, v2 offset:55808
	v_mul_f32_e32 v2, v6, v45
	v_cvt_pk_bf16_f32 v2, v2, s0
	ds_write_b16 v51, v2 offset:55872
	v_mul_f32_e32 v2, v23, v46
	v_cvt_pk_bf16_f32 v2, v2, s0
	ds_write_b16 v51, v2 offset:55936
	v_mul_f32_e32 v2, v7, v46
	v_cvt_pk_bf16_f32 v2, v2, s0
	ds_write_b16 v51, v2 offset:56000
	v_mul_f32_e32 v2, v24, v47
	v_cvt_pk_bf16_f32 v2, v2, s0
	ds_write_b16 v51, v2 offset:56576
	v_mul_f32_e32 v2, v8, v47
	v_cvt_pk_bf16_f32 v2, v2, s0
	ds_write_b16 v51, v2 offset:56640
	v_mul_f32_e32 v2, v25, v48
	v_cvt_pk_bf16_f32 v2, v2, s0
	ds_write_b16 v51, v2 offset:56704
	v_mul_f32_e32 v2, v9, v48
	v_cvt_pk_bf16_f32 v2, v2, s0
	ds_write_b16 v51, v2 offset:56768
	v_mul_f32_e32 v2, v26, v49
	v_cvt_pk_bf16_f32 v2, v2, s0
	ds_write_b16 v51, v2 offset:56832
	v_mul_f32_e32 v2, v10, v49
	v_cvt_pk_bf16_f32 v2, v2, s0
	s_waitcnt lgkmcnt(13)
	v_rcp_f32_e32 v36, v236
	ds_write_b16 v51, v2 offset:56896
	v_mul_f32_e32 v2, v27, v50
	v_cvt_pk_bf16_f32 v2, v2, s0
	ds_write_b16 v51, v2 offset:56960
	v_mul_f32_e32 v2, v11, v50
	v_cvt_pk_bf16_f32 v2, v2, s0
	v_rcp_f32_e32 v37, v237
	ds_write_b16 v51, v2 offset:57024
	v_mul_f32_e32 v2, v28, v36
	v_cvt_pk_bf16_f32 v2, v2, s0
	ds_write_b16 v51, v2 offset:57600
	v_mul_f32_e32 v2, v12, v36
	v_cvt_pk_bf16_f32 v2, v2, s0
	v_rcp_f32_e32 v38, v238
	ds_write_b16 v51, v2 offset:57664
	v_mul_f32_e32 v2, v29, v37
	v_cvt_pk_bf16_f32 v2, v2, s0
	ds_write_b16 v51, v2 offset:57728
	v_mul_f32_e32 v2, v13, v37
	v_cvt_pk_bf16_f32 v2, v2, s0
	v_rcp_f32_e32 v39, v239
	ds_write_b16 v51, v2 offset:57792
	v_mul_f32_e32 v2, v30, v38
	v_cvt_pk_bf16_f32 v2, v2, s0
	ds_write_b16 v51, v2 offset:57856
	v_mul_f32_e32 v2, v14, v38
	v_cvt_pk_bf16_f32 v2, v2, s0
	s_waitcnt lgkmcnt(14)
	v_rcp_f32_e32 v40, v240
	ds_write_b16 v51, v2 offset:57920
	v_mul_f32_e32 v2, v31, v39
	v_cvt_pk_bf16_f32 v2, v2, s0
	ds_write_b16 v51, v2 offset:57984
	v_mul_f32_e32 v2, v15, v39
	v_cvt_pk_bf16_f32 v2, v2, s0
	v_rcp_f32_e32 v41, v241
	ds_write_b16 v51, v2 offset:58048
	v_mul_f32_e32 v2, v32, v40
	v_cvt_pk_bf16_f32 v2, v2, s0
	ds_write_b16 v51, v2 offset:58624
	v_mul_f32_e32 v2, v16, v40
	v_cvt_pk_bf16_f32 v2, v2, s0
	v_rcp_f32_e32 v42, v242
	ds_write_b16 v51, v2 offset:58688
	v_mul_f32_e32 v2, v33, v41
	v_cvt_pk_bf16_f32 v2, v2, s0
	ds_write_b16 v51, v2 offset:58752
	v_mul_f32_e32 v2, v17, v41
	v_cvt_pk_bf16_f32 v2, v2, s0
	v_rcp_f32_e32 v43, v243
	ds_write_b16 v51, v2 offset:58816
	v_mul_f32_e32 v2, v34, v42
	v_cvt_pk_bf16_f32 v2, v2, s0
	ds_write_b16 v51, v2 offset:58880
	v_mul_f32_e32 v2, v18, v42
	v_cvt_pk_bf16_f32 v2, v2, s0
	ds_write_b16 v51, v2 offset:58944
	v_mul_f32_e32 v2, v35, v43
	v_cvt_pk_bf16_f32 v2, v2, s0
	ds_write_b16 v51, v2 offset:59008
	v_mul_f32_e32 v2, v19, v43
	v_cvt_pk_bf16_f32 v2, v2, s0
	ds_write_b16 v51, v2 offset:59072
	v_lshlrev_b32_e32 v2, 1, v212
	v_cvt_pk_bf16_f32 v20, v20, s0
	s_add_u32 s4, s4, s38
	v_and_b32_e32 v2, 0x70, v2
	ds_write_b16 v51, v20 offset:55552
	s_addc_u32 s5, s5, s39
	v_lshrrev_b32_e32 v1, 3, v1
	v_add_u32_e32 v16, s7, v2
	s_waitcnt lgkmcnt(0)
	v_lshl_add_u64 v[12:13], s[4:5], 0, v[2:3]
	v_lshl_add_u32 v2, v1, 7, v16
	v_or_b32_e32 v17, 8, v1
	ds_read_b128 v[4:7], v2 offset:55552
	v_lshl_add_u32 v8, v17, 7, v16
	ds_read_b128 v[8:11], v8 offset:55552
	v_lshlrev_b32_e32 v2, 11, v1
	v_lshl_add_u64 v[14:15], v[12:13], 0, v[2:3]
	v_lshlrev_b32_e32 v2, 11, v17
	s_waitcnt lgkmcnt(1)
	global_store_dwordx4 v[14:15], v[4:7], off
	s_add_i32 s55, s55, 1
	s_mov_b64 s[4:5], 0
	v_lshl_add_u64 v[4:5], v[12:13], 0, v[2:3]
	v_or_b32_e32 v2, 16, v1
	s_waitcnt lgkmcnt(0)
	global_store_dwordx4 v[4:5], v[8:11], off
	v_lshl_add_u32 v4, v2, 7, v16
	v_or_b32_e32 v1, 24, v1
	ds_read_b128 v[4:7], v4 offset:55552
	v_lshl_add_u32 v8, v1, 7, v16
	ds_read_b128 v[8:11], v8 offset:55552
	v_lshlrev_b32_e32 v2, 11, v2
	v_lshl_add_u64 v[14:15], v[12:13], 0, v[2:3]
	v_lshlrev_b32_e32 v2, 11, v1
	s_waitcnt lgkmcnt(1)
	global_store_dwordx4 v[14:15], v[4:7], off
	s_nop 1
	v_lshl_add_u64 v[4:5], v[12:13], 0, v[2:3]
	s_waitcnt lgkmcnt(0)
	global_store_dwordx4 v[4:5], v[8:11], off
	s_waitcnt lgkmcnt(0)
	s_barrier

;   #define DMA_K(t,slot) glds16(ksrc+(long)(t)*KVBLK*DM,(unsigned)__builtin_amdgcn_readfirstlane(kdst+(slot)))
;   #define DMA_V(t,slot) glds16(vsrc+(long)(t)*KVBLK*DM,(unsigned)__builtin_amdgcn_readfirstlane(vdst+(slot)))
;   #define WLOAD(W,t) asm volatile("global_load_dword %0, %1, off":"=v"(W):"v"(mwl+(size_t)(t)*64):"memory")
; template<int THRL> __device__ __forceinline__ void attn_unit(int b,int h,int qb,const bf16*Q,const bf16*__restrict__ K,const bf16*__restrict__ V,bf16*O,const unsigned*MASK,char*shm){
;   int tid_=threadIdx.x; asm volatile("":"+v"(tid_));
;   const int tid=tid_,lane=tid&63,r32=lane&31,hi=lane>>5; const int wid=__builtin_amdgcn_readfirstlane(tid>>6);
;   const long rowbase=(long)b*SEQ; const int q0=qb*QB;
;   const bf16*Qw=Q+(rowbase+q0+wid*QBLK)*DM+h*D;
;   const bf16*Kh=K+rowbase*DM+h*D,*Vh=V+rowbase*DM+h*D;
;   const unsigned lds0=(unsigned)(uintptr_t)shm;
;   float*wsf=(float*)(shm+LDS_WS)+wid*64;
;   const bf16*ksrc=Kh+(long)lane*DM+wid*8;
;   const bf16*vsrc=Vh+(long)(16*(wid&3)+(lane>>2))*DM+(wid>>2)*32+(lane&3)*8;
;   const unsigned kdst=lds0+LDS_K+wid*1024, vdst=lds0+LDS_V+wid*1024;
;     ...
;   const int vb0=(int)(lds0+LDS_V)+((lane>>4)&1)*32+(lane&3)*8+(4*hi+((lane&15)>>2))*64;
;   const char*Kbase=shm+LDS_K; bf16x8 kf[8];
;   const lds_cptr shm3=(lds_cptr)shm; const lds_cptr kp0=shm3+LDS_K+hi*1024+r32*16; const lds_cptr vp0=shm3+LDS_V+((lane>>4)&1)*32+(lane&3)*8+(4*hi+((lane&15)>>2))*64;
;   const int NT=(q0+QB)/KVBLK;
;   const unsigned*mwl=MASK+((size_t)(b*256+qb*8+wid)*128)*64+lane;
;   unsigned wA,wB;
;     ...
;   WLOAD(wA,0);WLOAD(wB,1);
;   DMA_K(0,0);DMA_V(0,0);DMA_K(1,SLOTB);
;   bf16x8 qr[4];
;   #pragma unroll
;   for(int d0=0;d0<4;++d0)qr[d0]=*reinterpret_cast<const bf16x8*>(&Qw[(long)r32*DM+d0*16+hi*8]);
.LBB0_1271:
	s_ashr_i32 s4, s6, 31
	s_lshr_b32 s4, s4, 29
	s_add_i32 s4, s6, s4
	s_ashr_i32 s42, s4, 3
	v_mov_b32_e32 v58, v0
	s_and_b32 s4, s4, 0x3fffff8
	s_ashr_i32 s43, s42, 31
	v_readfirstlane_b32 s50, v58
	s_lshl_b32 s51, s56, 8
	s_sub_i32 s38, s6, s4
	s_ashr_i32 s7, s50, 6
	s_lshl_b64 s[4:5], s[42:43], 13
	s_ashr_i32 s39, s51, 31
	s_add_u32 s4, s4, s51
	s_addc_u32 s5, s5, s39
	s_lshl_b32 s39, s7, 5
	s_ashr_i32 s40, s39, 31
	s_add_u32 s44, s4, s39
	s_addc_u32 s45, s5, s40
	s_lshl_b64 s[4:5], s[44:45], 10
	s_add_u32 s40, s8, s4
	s_addc_u32 s41, s9, s5
	s_lshl_b32 s4, s38, 6
	s_ashr_i32 s5, s4, 31
	s_lshl_b64 s[38:39], s[4:5], 1
	s_add_u32 s40, s40, s38
	s_addc_u32 s41, s41, s39
	s_lshl_b64 s[4:5], s[42:43], 23
	s_add_u32 s43, s17, s4
	s_addc_u32 s47, s18, s5
	s_add_u32 s46, s43, s38
	s_addc_u32 s47, s47, s39
	s_add_u32 s4, s19, s4
	v_and_b32_e32 v1, 63, v58
	s_addc_u32 s5, s20, s5
	s_add_u32 s48, s4, s38
	v_lshlrev_b32_e32 v2, 10, v1
	s_addc_u32 s49, s5, s39
	v_lshl_add_u64 v[4:5], s[46:47], 0, v[2:3]
	s_lshl_b32 s46, s7, 3
	s_lshl_b32 s4, s7, 4
	v_bfe_u32 v2, v58, 2, 4
	s_ashr_i32 s47, s46, 31
	v_and_or_b32 v2, s4, 48, v2
	s_ashr_i32 s4, s50, 3
	v_lshl_add_u64 v[194:195], s[46:47], 1, v[4:5]
	s_and_b32 s46, s4, 0xffffffe0
	s_and_b32 s5, s50, 0x3fffffc0
	s_ashr_i32 s47, s46, 31
	s_lshl_b32 s58, s7, 10
	s_cmp_lg_u32 0, -1
	s_cselect_b32 s4, 0, 0
	s_lshl_b32 s42, s42, 8
	s_lshl_b32 s43, s56, 3
	s_add_i32 s42, s42, s43
	s_add_i32 s42, s42, s7
	v_lshlrev_b32_e32 v2, 10, v2
	v_lshlrev_b32_e32 v212, 3, v58
	s_add_i32 s58, s58, s4
	s_ashr_i32 s43, s42, 31
	v_lshl_add_u64 v[4:5], s[48:49], 0, v[2:3]
	v_and_b32_e32 v215, 24, v212
	s_add_i32 s59, s58, 0x6000
	s_add_i32 s4, s51, 0x100
	s_lshl_b64 s[42:43], s[42:43], 15
	v_lshl_add_u64 v[4:5], s[46:47], 1, v[4:5]
	v_lshlrev_b32_e32 v2, 1, v215
	s_add_u32 s42, s23, s42
	v_lshl_add_u64 v[208:209], v[4:5], 0, v[2:3]
	s_addc_u32 s43, s54, s43
	v_lshlrev_b32_e32 v2, 2, v1
	v_lshl_add_u64 v[84:85], s[42:43], 0, v[2:3]
	global_load_dword v59, v[84:85], off
	s_waitcnt vmcnt(0)
	v_mul_u32_u24_sdwa v225, s32, v59 dst_sel:DWORD dst_unused:UNUSED_PAD src0_sel:DWORD src1_sel:BYTE_0
	v_and_b32_e32 v225, -16, v225
	v_mul_u32_u24_sdwa v226, s32, v59 dst_sel:DWORD dst_unused:UNUSED_PAD src0_sel:DWORD src1_sel:BYTE_1
	v_and_b32_e32 v226, -16, v226
	v_mul_u32_u24_sdwa v248, s32, v59 dst_sel:DWORD dst_unused:UNUSED_PAD src0_sel:DWORD src1_sel:BYTE_2
	v_and_b32_e32 v248, -16, v248
	v_mul_u32_u24_sdwa v249, s32, v59 dst_sel:DWORD dst_unused:UNUSED_PAD src0_sel:DWORD src1_sel:BYTE_3
	v_and_b32_e32 v249, -16, v249
	v_lshl_add_u64 v[186:187], v[84:85], 0, s[30:31]
	global_load_dword v218, v[186:187], off
	v_and_b32_e32 v213, 31, v58
	s_mov_b32 s42, m0
	s_mov_b32 m0, s58
	s_nop 0
	global_load_lds_dwordx4 v[194:195], off
	s_mov_b32 m0, s42
	v_bfe_u32 v214, v58, 5, 1
	s_mov_b32 s42, m0
	s_mov_b32 m0, s59
	s_nop 0
	global_load_lds_dwordx4 v[208:209], off
	s_mov_b32 m0, s42
	v_lshlrev_b32_e32 v2, 10, v213
	v_lshl_add_u64 v[4:5], v[194:195], 0, s[36:37]
	s_add_i32 s42, s58, 0x2000
	s_mov_b32 s43, m0
	s_mov_b32 m0, s42
	s_nop 0
	global_load_lds_dwordx4 v[4:5], off
	s_mov_b32 m0, s43
	v_lshl_or_b32 v2, v214, 4, v2
	global_load_dwordx4 v[138:141], v2, s[40:41]
	global_load_dwordx4 v[134:137], v2, s[40:41] offset:32
	global_load_dwordx4 v[126:129], v2, s[40:41] offset:64
	global_load_dwordx4 v[122:125], v2, s[40:41] offset:96
	v_mov_b32_e32 v228, 0
	v_mov_b32_e32 v229, 0
	v_mov_b32_e32 v230, 0
	v_mov_b32_e32 v231, 0
	v_mov_b32_e32 v232, 0
	v_mov_b32_e32 v233, 0
	v_mov_b32_e32 v234, 0
	v_mov_b32_e32 v235, 0
	v_mov_b32_e32 v236, 0
	v_mov_b32_e32 v237, 0
	v_mov_b32_e32 v238, 0
	v_mov_b32_e32 v239, 0
	v_mov_b32_e32 v240, 0
	v_mov_b32_e32 v241, 0
	v_mov_b32_e32 v242, 0
	v_mov_b32_e32 v243, 0
	v_mov_b32_e32 v16, v3
	v_mov_b32_e32 v17, v3
	v_lshlrev_b32_e32 v2, 10, v214
	v_lshlrev_b32_e32 v18, 4, v213
	v_mov_b32_e32 v4, v3
	v_mov_b32_e32 v5, v3
	v_mov_b32_e32 v6, v3
	v_mov_b32_e32 v7, v3
	v_mov_b32_e32 v8, v3
	v_mov_b32_e32 v9, v3
	v_mov_b32_e32 v10, v3
	v_mov_b32_e32 v11, v3
	v_mov_b32_e32 v12, v3
	v_mov_b32_e32 v13, v3
	v_mov_b32_e32 v14, v3
	v_mov_b32_e32 v15, v3
	v_add3_u32 v221, 0, v2, v18
	v_mov_b32_e32 v2, v3
	v_mov_b64_e32 v[32:33], v[16:17]
	v_mov_b64_e32 v[30:31], v[14:15]
	v_mov_b64_e32 v[28:29], v[12:13]
	v_mov_b64_e32 v[26:27], v[10:11]
	v_mov_b64_e32 v[24:25], v[8:9]
	v_mov_b64_e32 v[22:23], v[6:7]
	v_mov_b64_e32 v[20:21], v[4:5]
	v_mov_b64_e32 v[18:19], v[2:3]
	v_lshl_add_u64 v[34:35], v[194:195], 0, s[0:1]
	s_add_i32 s40, s58, 0x4000
	s_mov_b32 s41, m0
	s_mov_b32 m0, s40
	s_nop 0
	global_load_lds_dwordx4 v[34:35], off
	s_mov_b32 m0, s41
	s_waitcnt vmcnt(3) lgkmcnt(0)
	s_barrier
; #define MASK1(p,w,e) ({ unsigned m_; asm("v_bfe_i32 %0, %1, %2, 1":"=v"(m_):"v"(w),"n"(e)); __uint_as_float(__float_as_uint(p)&m_); })
; #define WAIT_BAR(N) asm volatile("s_waitcnt vmcnt(" #N ") lgkmcnt(0)\n\ts_barrier":::"memory")
;   #define DMA_K(t,slot) glds16(ksrc+(long)(t)*KVBLK*DM,(unsigned)__builtin_amdgcn_readfirstlane(kdst+(slot)))
; __device__ __forceinline__ void qkt(f32x16&p0,f32x16&p1,const char*Kslot,const bf16x8*qr,const f32x16&negm,int r32,int hi){
;   const char*kb=Kslot+hi*1024+r32*16;
;   #pragma unroll
;   for(int d0=0;d0<4;++d0){
;     const bf16x8 b0=*reinterpret_cast<const bf16x8*>(kb+d0*2048);
;     const bf16x8 b1=*reinterpret_cast<const bf16x8*>(kb+d0*2048+512);
;     if(d0==0){p0=__builtin_amdgcn_mfma_f32_32x32x16_bf16(b0,qr[0],negm,0,0,0);p1=__builtin_amdgcn_mfma_f32_32x32x16_bf16(b1,qr[0],negm,0,0,0);}
;     else{p0=__builtin_amdgcn_mfma_f32_32x32x16_bf16(b0,qr[d0],p0,0,0,0);p1=__builtin_amdgcn_mfma_f32_32x32x16_bf16(b1,qr[d0],p1,0,0,0);}}
; }
; template<int THRL> __device__ __forceinline__ void attn_unit(int b,int h,int qb,const bf16*Q,const bf16*__restrict__ K,const bf16*__restrict__ V,bf16*O,const unsigned*MASK,char*shm){
;     ...
;   DMA_K(2,2*SLOTB);
;   WAIT_BAR(3);
;   qkt(pA0,pA1,Kbase,qr,negm,r32,hi);asm volatile("s_nop 15\n\ts_nop 7":"+v"(pA0),"+v"(pA1));
;   START(pA0,pA1);
;   _Pragma("unroll") for(int r=0;r<16;++r)pA1[r]=__builtin_amdgcn_exp2f(pA1[r]);
;   _Pragma("unroll") for(int r=0;r<16;++r){pA0[r]=MASK1(pA0[r],wA,r);pA1[r]=MASK1(pA1[r],wA,16+r);}
	ds_read_b128 v[50:53], v221
	ds_read_b128 v[54:57], v221 offset:512
	s_mov_b32 s40, 0xf149f2ca
	s_waitcnt vmcnt(3) lgkmcnt(1)
	v_mfma_f32_32x32x16_bf16 v[34:49], v[50:53], v[138:141], v[18:33]
	v_bfe_i32 v70, v59, 3, 1
	v_bfe_i32 v71, v59, 4, 1
	v_bfe_i32 v72, v59, 5, 1
	v_bfe_i32 v73, v59, 6, 1
	v_bfe_i32 v74, v59, 7, 1
	v_bfe_i32 v75, v59, 8, 1
	v_bfe_i32 v76, v59, 9, 1
	s_waitcnt lgkmcnt(0)
	v_mfma_f32_32x32x16_bf16 v[18:33], v[54:57], v[138:141], v[18:33]
	ds_read_b128 v[50:53], v221 offset:2048
	ds_read_b128 v[54:57], v221 offset:2560
	v_bfe_i32 v77, v59, 10, 1
	v_bfe_i32 v78, v59, 11, 1
	v_bfe_i32 v79, v59, 12, 1
	v_bfe_i32 v80, v59, 13, 1
	v_bfe_i32 v81, v59, 14, 1
	v_bfe_i32 v82, v59, 15, 1
	s_waitcnt vmcnt(2) lgkmcnt(1)
	v_mfma_f32_32x32x16_bf16 v[34:49], v[50:53], v[134:137], v[34:49]
	s_lshl_b32 s5, s5, 2
	v_bfe_i32 v86, v59, 16, 1
	v_bfe_i32 v87, v59, 17, 1
	v_bfe_i32 v69, v59, 2, 1
	s_ashr_i32 s61, s4, 6
	s_add_i32 s57, s5, 0
	v_bfe_i32 v67, v59, 0, 1
	s_waitcnt lgkmcnt(0)
	v_mfma_f32_32x32x16_bf16 v[18:33], v[54:57], v[134:137], v[18:33]
	ds_read_b128 v[50:53], v221 offset:4096
	ds_read_b128 v[54:57], v221 offset:4608
	v_bfe_i32 v68, v59, 1, 1
	s_mov_b32 s92, 1
	s_mov_b32 s48, 0
	s_movk_i32 s60, 0x2000
	s_movk_i32 s62, 0x4000
	v_bfe_i32 v88, v59, 18, 1
	s_waitcnt vmcnt(1) lgkmcnt(1)
	v_mfma_f32_32x32x16_bf16 v[34:49], v[50:53], v[126:129], v[34:49]
	ds_read_b128 v[50:53], v221 offset:6144
	v_bfe_i32 v89, v59, 19, 1
	v_bfe_i32 v90, v59, 20, 1
	v_bfe_i32 v91, v59, 21, 1
	v_bfe_i32 v92, v59, 22, 1
	v_bfe_i32 v93, v59, 23, 1
	v_bfe_i32 v94, v59, 24, 1
	s_waitcnt lgkmcnt(1)
	v_mfma_f32_32x32x16_bf16 v[18:33], v[54:57], v[126:129], v[18:33]
	ds_read_b128 v[54:57], v221 offset:6656
	v_bfe_i32 v95, v59, 25, 1
	v_bfe_i32 v96, v59, 26, 1
	v_bfe_i32 v97, v59, 27, 1
	v_bfe_i32 v98, v59, 28, 1
	v_bfe_i32 v99, v59, 29, 1
	v_bfe_i32 v100, v59, 30, 1
	s_waitcnt vmcnt(0) lgkmcnt(1)
	v_mfma_f32_32x32x16_bf16 v[34:49], v[50:53], v[122:125], v[34:49]
	v_lshlrev_b32_e32 v50, 1, v58
	v_lshlrev_b32_e32 v51, 4, v58
	v_and_b32_e32 v217, 32, v50
	v_and_b32_e32 v50, 0xc0, v51
	v_lshl_or_b32 v216, v214, 8, v50
	v_add_u32_e32 v50, 0, v217
	v_add3_u32 v220, v50, v215, v216
	s_waitcnt lgkmcnt(0)
	v_mfma_f32_32x32x16_bf16 v[18:33], v[54:57], v[122:125], v[18:33]
	s_nop 15
	s_nop 7
	s_nop 0
	v_max3_f32 v50, v34, v35, v18
	v_max3_f32 v51, v36, v37, v19
	s_nop 0
	v_max3_f32 v50, v50, v20, v21
	v_max3_f32 v51, v51, v40, v41
	s_nop 0
	v_max3_f32 v50, v50, v38, v39
	v_max3_f32 v51, v51, v24, v25
	s_nop 0
	v_max3_f32 v50, v50, v22, v23
	v_max3_f32 v51, v51, v44, v45
	s_nop 0
	v_max3_f32 v50, v50, v42, v43
	v_max3_f32 v51, v51, v28, v29
	s_nop 0
	v_max3_f32 v50, v50, v26, v27
	v_max3_f32 v51, v51, v48, v49
	s_nop 0
	v_max3_f32 v50, v50, v46, v47
	v_max3_f32 v51, v51, v32, v33
	s_nop 0
	v_max3_f32 v50, v50, v30, v31
	s_nop 0
	v_max_f32_e32 v50, v50, v51
	s_nop 0
	v_mov_b32_e32 v51, v50
	s_nop 1
	v_permlane32_swap_b32_e32 v50, v51
	v_max_f32_e32 v50, v50, v51
	s_nop 0
	v_cmp_lt_f32_e32 vcc, s40, v50
	v_cmp_gt_u32_e64 s[40:41], 32, v1
	s_nop 0
	v_cndmask_b32_e32 v50, 0, v50, vcc
	v_sub_f32_e32 v18, v18, v50
	v_sub_f32_e32 v19, v19, v50
	v_sub_f32_e32 v52, v36, v50
	v_sub_f32_e32 v53, v37, v50
	v_sub_f32_e32 v54, v38, v50
	v_sub_f32_e32 v55, v39, v50
	v_sub_f32_e32 v56, v40, v50
	v_sub_f32_e32 v57, v41, v50
	v_sub_f32_e32 v58, v42, v50
	v_sub_f32_e32 v60, v43, v50
	v_sub_f32_e32 v61, v44, v50
	v_sub_f32_e32 v62, v45, v50
	v_sub_f32_e32 v63, v46, v50
	v_sub_f32_e32 v64, v47, v50
	v_sub_f32_e32 v65, v48, v50
	v_sub_f32_e32 v66, v49, v50
	s_nop 0
	v_exp_f32_e32 v52, v52
	v_exp_f32_e32 v53, v53
	v_exp_f32_e32 v54, v54
	v_exp_f32_e32 v55, v55
	v_exp_f32_e32 v56, v56
	v_exp_f32_e32 v57, v57
	v_exp_f32_e32 v58, v58
	v_exp_f32_e32 v60, v60
	v_exp_f32_e32 v61, v61
	v_exp_f32_e32 v62, v62
	v_exp_f32_e32 v63, v63
	v_exp_f32_e32 v64, v64
	v_exp_f32_e32 v65, v65
	v_exp_f32_e32 v66, v66
	v_exp_f32_e32 v18, v18
	v_exp_f32_e32 v19, v19
	v_add_f32_e32 v219, v3, v50
	v_sub_f32_e32 v34, v34, v50
	v_sub_f32_e32 v35, v35, v50
	v_sub_f32_e32 v20, v20, v50
	v_sub_f32_e32 v21, v21, v50
	v_sub_f32_e32 v22, v22, v50
	s_nop 0
	v_xor_b32_e32 v36, 0x80000000, v219
	v_sub_f32_e32 v23, v23, v50
	v_sub_f32_e32 v24, v24, v50
	v_sub_f32_e32 v25, v25, v50
	v_sub_f32_e32 v26, v26, v50
	v_sub_f32_e32 v27, v27, v50
	v_sub_f32_e32 v28, v28, v50
	v_sub_f32_e32 v29, v29, v50
	v_sub_f32_e32 v30, v30, v50
	v_sub_f32_e32 v31, v31, v50
	v_sub_f32_e32 v32, v32, v50
	v_sub_f32_e32 v33, v33, v50
	v_mov_b32_e32 v37, v36
	v_mov_b32_e32 v38, v36
	v_mov_b32_e32 v39, v36
	v_mov_b32_e32 v40, v36
	v_mov_b32_e32 v41, v36
	v_mov_b32_e32 v42, v36
	v_mov_b32_e32 v43, v36
	v_mov_b32_e32 v44, v36
	v_mov_b32_e32 v45, v36
	v_mov_b32_e32 v46, v36
	v_mov_b32_e32 v47, v36
	v_mov_b32_e32 v48, v36
	v_mov_b32_e32 v49, v36
	v_mov_b32_e32 v50, v36
	v_mov_b32_e32 v51, v36
	s_waitcnt vmcnt(0) lgkmcnt(0)
	s_barrier
; #define MASK1(p,w,e) ({ unsigned m_; asm("v_bfe_i32 %0, %1, %2, 1":"=v"(m_):"v"(w),"n"(e)); __uint_as_float(__float_as_uint(p)&m_); })
; #define WAIT_BAR(N) asm volatile("s_waitcnt vmcnt(" #N ") lgkmcnt(0)\n\ts_barrier":::"memory")
;   #define DMA_K(t,slot) glds16(ksrc+(long)(t)*KVBLK*DM,(unsigned)__builtin_amdgcn_readfirstlane(kdst+(slot)))
;   #define DMA_V(t,slot) glds16(vsrc+(long)(t)*KVBLK*DM,(unsigned)__builtin_amdgcn_readfirstlane(vdst+(slot)))
;   #define ROT() do{sl_prev=sl_cur;sl_cur=sl_next;sl_next=(sl_next==(NSLOT-1)*SLOTB)?0:sl_next+SLOTB;}while(0)
; template<int THRL> __device__ __forceinline__ void attn_unit(int b,int h,int qb,const bf16*Q,const bf16*__restrict__ K,const bf16*__restrict__ V,bf16*O,const unsigned*MASK,char*shm){
;     ...
;   _Pragma("unroll") for(int r=0;r<16;++r){pA0[r]=MASK1(pA0[r],wA,r);pA1[r]=MASK1(pA1[r],wA,16+r);}
;   WAIT_BAR(0);
;   DMA_K(3,0);DMA_V(1,SLOTB);
;   ROT();
;   kload8(kf,kp0+sl_cur);
;   WAIT_BAR(2);
;   s16x4 vlo[8],vhi[8]; u32x4 pw0,pw1,pw2,pw3;
;     ...
;   int t=1;
;   for(;t+5<NT;t+=2){
	v_and_b32_e32 v83, v82, v66
	v_and_b32_e32 v82, v81, v65
	v_and_b32_e32 v81, v80, v64
	v_and_b32_e32 v80, v79, v63
	v_and_b32_e32 v79, v78, v62
	v_and_b32_e32 v78, v77, v61
	v_and_b32_e32 v77, v76, v60
	v_and_b32_e32 v76, v75, v58
	v_and_b32_e32 v75, v74, v57
	v_and_b32_e32 v74, v73, v56
	v_and_b32_e32 v73, v72, v55
	v_and_b32_e32 v72, v71, v54
	v_and_b32_e32 v71, v70, v53
	v_and_b32_e32 v70, v69, v52
	v_and_b32_e32 v53, v87, v19
	v_and_b32_e32 v52, v86, v18
	v_lshl_add_u64 v[18:19], v[194:195], 0, s[82:83]
	s_mov_b32 s4, m0
	s_mov_b32 m0, s58
	s_nop 0
	global_load_lds_dwordx4 v[18:19], off
	s_mov_b32 m0, s4
	v_lshl_add_u64 v[18:19], v[208:209], 0, s[36:37]
	s_add_i32 s4, s58, 0x8000
	s_mov_b32 s5, m0
	s_mov_b32 m0, s4
	s_nop 0
	global_load_lds_dwordx4 v[18:19], off
	s_mov_b32 m0, s5
	ds_read_b128 v[178:181], v221 offset:8192
	ds_read_b128 v[170:173], v221 offset:8704
	ds_read_b128 v[174:177], v221 offset:10240
	ds_read_b128 v[162:165], v221 offset:10752
	ds_read_b128 v[166:169], v221 offset:12288
	ds_read_b128 v[154:157], v221 offset:12800
	ds_read_b128 v[158:161], v221 offset:14336
	ds_read_b128 v[150:153], v221 offset:14848
	v_exp_f32_e32 v34, v34
	v_exp_f32_e32 v35, v35
	v_exp_f32_e32 v20, v20
	v_exp_f32_e32 v21, v21
	v_exp_f32_e32 v22, v22
	v_exp_f32_e32 v23, v23
	v_exp_f32_e32 v24, v24
	v_exp_f32_e32 v25, v25
	v_exp_f32_e32 v26, v26
	v_exp_f32_e32 v27, v27
	v_exp_f32_e32 v28, v28
	v_exp_f32_e32 v29, v29
	v_exp_f32_e32 v30, v30
	v_exp_f32_e32 v31, v31
	v_exp_f32_e32 v32, v32
	v_exp_f32_e32 v33, v33
	s_waitcnt vmcnt(2) lgkmcnt(0)
	s_barrier
	v_and_b32_e32 v69, v68, v35
	v_and_b32_e32 v68, v67, v34
	v_bfe_i32 v34, v59, 31, 1
	v_and_b32_e32 v66, v100, v32
	v_and_b32_e32 v67, v34, v33
	v_and_b32_e32 v65, v99, v31
	v_and_b32_e32 v64, v98, v30
	v_and_b32_e32 v63, v97, v29
	v_and_b32_e32 v62, v96, v28
	v_and_b32_e32 v61, v95, v27
	v_and_b32_e32 v60, v94, v26
	v_and_b32_e32 v59, v93, v25
	v_and_b32_e32 v58, v92, v24
	v_and_b32_e32 v57, v91, v23
	v_and_b32_e32 v56, v90, v22
	v_and_b32_e32 v55, v89, v21
	v_and_b32_e32 v54, v88, v20
	s_cmp_lt_i32 s61, 7
	s_cbranch_scc1 .LBB0_1287
	s_mov_b64 s[4:5], 0x50000
	v_lshlrev_b32_e32 v18, 4, v214
	v_lshl_add_u64 v[188:189], v[194:195], 0, s[4:5]
	s_mov_b64 s[4:5], 0x300
	v_mov_b64_e32 v[34:35], v[16:17]
	v_lshl_add_u64 v[192:193], v[84:85], 0, s[4:5]
	v_add_u32_e32 v85, s57, v18
	v_mov_b64_e32 v[32:33], v[14:15]
	v_mov_b64_e32 v[30:31], v[12:13]
	v_mov_b64_e32 v[28:29], v[10:11]
	v_mov_b64_e32 v[26:27], v[8:9]
	v_mov_b64_e32 v[24:25], v[6:7]
	v_mov_b64_e32 v[22:23], v[4:5]
	v_mov_b64_e32 v[20:21], v[2:3]
	v_mov_b64_e32 v[18:19], v[16:17]
	s_add_i32 s46, s61, -5
	v_lshl_add_u32 v210, v213, 2, s57
	v_lshl_add_u64 v[190:191], v[208:209], 0, s[82:83]
	s_mov_b32 s4, 0
	s_movk_i32 s48, 0x4000
	s_movk_i32 s47, 0x2000
	v_mov_b32_e32 v84, 0
	v_mov_b64_e32 v[16:17], v[14:15]
	v_mov_b64_e32 v[14:15], v[12:13]
	v_mov_b64_e32 v[12:13], v[10:11]
	v_mov_b64_e32 v[10:11], v[8:9]
	v_mov_b64_e32 v[8:9], v[6:7]
	v_mov_b64_e32 v[6:7], v[4:5]
	v_mov_b64_e32 v[4:5], v[2:3]

; #define WAIT_BAR(N) asm volatile("s_waitcnt vmcnt(" #N ") lgkmcnt(0)\n\ts_barrier":::"memory")
;   #define RESC() do{ if(resc){ asm volatile("s_waitcnt lgkmcnt(0)":::"memory"); \
;       _Pragma("unroll") for(int d_=0;d_<2;++d_) _Pragma("unroll") for(int r=0;r<16;++r)o[d_][r]*=wsf[crow(r,hi)]; } }while(0)
;   #define ROT() do{sl_prev=sl_cur;sl_cur=sl_next;sl_next=(sl_next==(NSLOT-1)*SLOTB)?0:sl_next+SLOTB;}while(0)
; template<int THRL> __device__ __forceinline__ void attn_unit(int b,int h,int qb,const bf16*Q,const bf16*__restrict__ K,const bf16*__restrict__ V,bf16*O,const unsigned*MASK,char*shm){
;     ...
;   int t=1;
;   for(;t+5<NT;t+=2){
;     STEP(pB0,pB1,pA0,pA1,t,true,true,true,wB,wA);     WAIT_BAR(2); RESC(); ROT();
.LBB0_1274:
	s_waitcnt lgkmcnt(0)
	v_and_b32_e32 v146, v146, v80
	v_and_b32_e32 v147, v147, v81
	v_and_b32_e32 v148, v148, v82
	v_and_b32_e32 v149, v149, v83
	ds_read_b128 v[80:83], v226 offset:51200
	s_waitcnt lgkmcnt(14)
	v_mfma_f32_32x32x16_bf16 v[20:35], v[146:149], v[182:185], v[20:35]
	v_exp_f32_e32 v102, v102
	v_exp_f32_e32 v103, v103
	v_exp_f32_e32 v104, v104
	v_exp_f32_e32 v105, v105
	s_waitcnt lgkmcnt(12)
	v_mfma_f32_32x32x16_bf16 v[4:19], v[146:149], v[178:181], v[4:19]
	v_mfma_f32_32x32x16_bf16 v[228:243], v[146:149], v[204:207], v[228:243]
	v_exp_f32_e32 v106, v106
	v_exp_f32_e32 v107, v107
	v_exp_f32_e32 v108, v108
	v_exp_f32_e32 v109, v109
	s_waitcnt lgkmcnt(0)
	v_and_b32_e32 v142, v142, v80
	v_and_b32_e32 v143, v143, v81
	v_and_b32_e32 v144, v144, v82
	v_and_b32_e32 v145, v145, v83
	ds_read_b128 v[80:83], v248 offset:51200
	v_add_u32_e32 v64, s48, v221
	ds_read_b128 v[60:63], v64
	ds_read_b128 v[150:153], v64 offset:512
	s_waitcnt lgkmcnt(12)
	v_mfma_f32_32x32x16_bf16 v[20:35], v[142:145], v[170:173], v[20:35]
	v_exp_f32_e32 v110, v110
	v_exp_f32_e32 v111, v111
	v_exp_f32_e32 v112, v112
	v_exp_f32_e32 v113, v113
	ds_read_b128 v[174:177], v64 offset:2048
	ds_read_b128 v[162:165], v64 offset:2560
	s_waitcnt lgkmcnt(12)
	v_mfma_f32_32x32x16_bf16 v[4:19], v[142:145], v[76:79], v[4:19]
	v_mfma_f32_32x32x16_bf16 v[228:243], v[142:145], v[204:207], v[228:243]
	v_exp_f32_e32 v114, v114
	v_exp_f32_e32 v115, v115
	v_exp_f32_e32 v116, v116
	v_exp_f32_e32 v117, v117
	s_waitcnt lgkmcnt(4)
	v_and_b32_e32 v130, v130, v80
	v_and_b32_e32 v131, v131, v81
	v_and_b32_e32 v132, v132, v82
	v_and_b32_e32 v133, v133, v83
	ds_read_b128 v[80:83], v249 offset:51200
	ds_read_b128 v[170:173], v64 offset:4096
	ds_read_b128 v[158:161], v64 offset:4608
	s_waitcnt lgkmcnt(12)
	v_mfma_f32_32x32x16_bf16 v[20:35], v[130:133], v[72:75], v[20:35]
	v_exp_f32_e32 v86, v86
	v_exp_f32_e32 v87, v87
	v_exp_f32_e32 v88, v88
	v_exp_f32_e32 v89, v89
	ds_read_b128 v[166:169], v64 offset:6144
	ds_read_b128 v[154:157], v64 offset:6656
	s_waitcnt lgkmcnt(12)
	v_mfma_f32_32x32x16_bf16 v[4:19], v[130:133], v[68:71], v[4:19]
	v_mfma_f32_32x32x16_bf16 v[228:243], v[130:133], v[204:207], v[228:243]
	v_exp_f32_e32 v90, v90
	v_exp_f32_e32 v91, v91
	v_exp_f32_e32 v92, v92
	v_exp_f32_e32 v93, v93
	s_waitcnt lgkmcnt(4)
	v_and_b32_e32 v118, v118, v80
	v_and_b32_e32 v119, v119, v81
	v_and_b32_e32 v120, v120, v82
	v_and_b32_e32 v121, v121, v83
	s_nop 0
	s_waitcnt lgkmcnt(10)
	v_mfma_f32_32x32x16_bf16 v[20:35], v[118:121], v[56:59], v[20:35]
	v_exp_f32_e32 v94, v94
	v_exp_f32_e32 v95, v95
	v_exp_f32_e32 v96, v96
	v_exp_f32_e32 v97, v97
	s_waitcnt lgkmcnt(8)
	v_mfma_f32_32x32x16_bf16 v[4:19], v[118:121], v[52:55], v[4:19]
	v_mfma_f32_32x32x16_bf16 v[228:243], v[118:121], v[204:207], v[228:243]
	v_exp_f32_e32 v98, v98
	v_exp_f32_e32 v99, v99
	v_exp_f32_e32 v100, v100
	v_exp_f32_e32 v101, v101
	s_waitcnt vmcnt(3)
	v_mul_u32_u24_sdwa v225, s32, v218 dst_sel:DWORD dst_unused:UNUSED_PAD src0_sel:DWORD src1_sel:BYTE_0
	v_and_b32_e32 v225, -16, v225
	v_mul_u32_u24_sdwa v226, s32, v218 dst_sel:DWORD dst_unused:UNUSED_PAD src0_sel:DWORD src1_sel:BYTE_1
	v_and_b32_e32 v226, -16, v226
	v_mul_u32_u24_sdwa v248, s32, v218 dst_sel:DWORD dst_unused:UNUSED_PAD src0_sel:DWORD src1_sel:BYTE_2
	v_and_b32_e32 v248, -16, v248
	v_mul_u32_u24_sdwa v249, s32, v218 dst_sel:DWORD dst_unused:UNUSED_PAD src0_sel:DWORD src1_sel:BYTE_3
	v_and_b32_e32 v249, -16, v249
	s_waitcnt vmcnt(3) lgkmcnt(0)
	s_barrier
	s_andn2_b64 vcc, exec, s[42:43]
	s_cbranch_vccnz .LBB0_1276
	s_waitcnt lgkmcnt(0)
	ds_read_b128 v[52:55], v85 offset:49248
	ds_read_b128 v[56:59], v85 offset:49216
	ds_read_b128 v[64:67], v85 offset:49184
	ds_read_b128 v[68:71], v85 offset:49152
	s_waitcnt lgkmcnt(3)
	v_pk_mul_f32 v[32:33], v[32:33], v[52:53]
	s_waitcnt lgkmcnt(2)
	v_pk_mul_f32 v[28:29], v[28:29], v[56:57]
	s_waitcnt lgkmcnt(1)
	v_pk_mul_f32 v[24:25], v[24:25], v[64:65]
	v_pk_mul_f32 v[34:35], v[34:35], v[54:55]
	v_pk_mul_f32 v[30:31], v[30:31], v[58:59]
	v_pk_mul_f32 v[26:27], v[26:27], v[66:67]
	s_waitcnt lgkmcnt(0)
	v_pk_mul_f32 v[22:23], v[22:23], v[70:71]
	v_pk_mul_f32 v[20:21], v[20:21], v[68:69]
	v_pk_mul_f32 v[16:17], v[16:17], v[52:53]
	v_pk_mul_f32 v[12:13], v[12:13], v[56:57]
	v_pk_mul_f32 v[8:9], v[8:9], v[64:65]
	v_pk_mul_f32 v[18:19], v[18:19], v[54:55]
	v_pk_mul_f32 v[14:15], v[14:15], v[58:59]
	v_pk_mul_f32 v[10:11], v[10:11], v[66:67]
	v_pk_mul_f32 v[6:7], v[6:7], v[70:71]
	v_pk_mul_f32 v[4:5], v[4:5], v[68:69]
	v_pk_mul_f32 v[240:241], v[240:241], v[52:53]
	v_pk_mul_f32 v[236:237], v[236:237], v[56:57]
	v_pk_mul_f32 v[232:233], v[232:233], v[64:65]
	v_pk_mul_f32 v[242:243], v[242:243], v[54:55]
	v_pk_mul_f32 v[238:239], v[238:239], v[58:59]
	v_pk_mul_f32 v[234:235], v[234:235], v[66:67]
	v_pk_mul_f32 v[230:231], v[230:231], v[70:71]
	v_pk_mul_f32 v[228:229], v[228:229], v[68:69]

; #define WAIT_BAR(N) asm volatile("s_waitcnt vmcnt(" #N ") lgkmcnt(0)\n\ts_barrier":::"memory")
;   #define RESC() do{ if(resc){ asm volatile("s_waitcnt lgkmcnt(0)":::"memory"); \
;       _Pragma("unroll") for(int d_=0;d_<2;++d_) _Pragma("unroll") for(int r=0;r<16;++r)o[d_][r]*=wsf[crow(r,hi)]; } }while(0)
;   #define ROT() do{sl_prev=sl_cur;sl_cur=sl_next;sl_next=(sl_next==(NSLOT-1)*SLOTB)?0:sl_next+SLOTB;}while(0)
; template<int THRL> __device__ __forceinline__ void attn_unit(int b,int h,int qb,const bf16*Q,const bf16*__restrict__ K,const bf16*__restrict__ V,bf16*O,const unsigned*MASK,char*shm){
;     ...
;   int t=1;
;   for(;t+5<NT;t+=2){
;     STEP(pB0,pB1,pA0,pA1,t,true,true,true,wB,wA);     WAIT_BAR(2); RESC(); ROT();
;     STEP(pA0,pA1,pB0,pB1,t+1,true,true,true,wA,wB);   WAIT_BAR(2); RESC(); ROT();
.LBB0_1277:
	s_waitcnt lgkmcnt(0)
	v_and_b32_e32 v146, v146, v114
	v_and_b32_e32 v147, v147, v115
	v_and_b32_e32 v148, v148, v116
	v_and_b32_e32 v149, v149, v117
	ds_read_b128 v[114:117], v226 offset:51200
	s_waitcnt lgkmcnt(14)
	v_mfma_f32_32x32x16_bf16 v[20:35], v[146:149], v[182:185], v[20:35]
	v_exp_f32_e32 v68, v68
	v_exp_f32_e32 v69, v69
	v_exp_f32_e32 v70, v70
	v_exp_f32_e32 v71, v71
	s_waitcnt lgkmcnt(12)
	v_mfma_f32_32x32x16_bf16 v[4:19], v[146:149], v[178:181], v[4:19]
	v_mfma_f32_32x32x16_bf16 v[228:243], v[146:149], v[204:207], v[228:243]
	v_exp_f32_e32 v72, v72
	v_exp_f32_e32 v73, v73
	v_exp_f32_e32 v74, v74
	v_exp_f32_e32 v75, v75
	s_waitcnt lgkmcnt(0)
	v_and_b32_e32 v142, v142, v114
	v_and_b32_e32 v143, v143, v115
	v_and_b32_e32 v144, v144, v116
	v_and_b32_e32 v145, v145, v117
	ds_read_b128 v[114:117], v248 offset:51200
	v_add_u32_e32 v94, s60, v221
	ds_read_b128 v[178:181], v94
	ds_read_b128 v[170:173], v94 offset:512
	s_waitcnt lgkmcnt(12)
	v_mfma_f32_32x32x16_bf16 v[20:35], v[142:145], v[150:153], v[20:35]
	v_exp_f32_e32 v76, v76
	v_exp_f32_e32 v77, v77
	v_exp_f32_e32 v78, v78
	v_exp_f32_e32 v79, v79
	ds_read_b128 v[174:177], v94 offset:2048
	ds_read_b128 v[162:165], v94 offset:2560
	s_waitcnt lgkmcnt(12)
	v_mfma_f32_32x32x16_bf16 v[4:19], v[142:145], v[110:113], v[4:19]
	v_mfma_f32_32x32x16_bf16 v[228:243], v[142:145], v[204:207], v[228:243]
	v_exp_f32_e32 v80, v80
	v_exp_f32_e32 v81, v81
	v_exp_f32_e32 v82, v82
	v_exp_f32_e32 v83, v83
	s_waitcnt lgkmcnt(4)
	v_and_b32_e32 v130, v130, v114
	v_and_b32_e32 v131, v131, v115
	v_and_b32_e32 v132, v132, v116
	v_and_b32_e32 v133, v133, v117
	ds_read_b128 v[114:117], v249 offset:51200
	ds_read_b128 v[166:169], v94 offset:4096
	ds_read_b128 v[154:157], v94 offset:4608
	s_waitcnt lgkmcnt(12)
	v_mfma_f32_32x32x16_bf16 v[20:35], v[130:133], v[106:109], v[20:35]
	v_exp_f32_e32 v52, v52
	v_exp_f32_e32 v53, v53
	v_exp_f32_e32 v54, v54
	v_exp_f32_e32 v55, v55
	ds_read_b128 v[158:161], v94 offset:6144
	ds_read_b128 v[150:153], v94 offset:6656
	s_waitcnt lgkmcnt(12)
	v_mfma_f32_32x32x16_bf16 v[4:19], v[130:133], v[102:105], v[4:19]
	v_mfma_f32_32x32x16_bf16 v[228:243], v[130:133], v[204:207], v[228:243]
	v_exp_f32_e32 v56, v56
	v_exp_f32_e32 v57, v57
	v_exp_f32_e32 v58, v58
	v_exp_f32_e32 v59, v59
	s_waitcnt lgkmcnt(4)
	v_and_b32_e32 v118, v118, v114
	v_and_b32_e32 v119, v119, v115
	v_and_b32_e32 v120, v120, v116
	v_and_b32_e32 v121, v121, v117
	s_nop 0
	s_waitcnt lgkmcnt(10)
	v_mfma_f32_32x32x16_bf16 v[20:35], v[118:121], v[90:93], v[20:35]
	v_exp_f32_e32 v60, v60
	v_exp_f32_e32 v61, v61
	v_exp_f32_e32 v62, v62
	v_exp_f32_e32 v63, v63
	s_waitcnt lgkmcnt(8)
	v_mfma_f32_32x32x16_bf16 v[4:19], v[118:121], v[86:89], v[4:19]
	v_mfma_f32_32x32x16_bf16 v[228:243], v[118:121], v[204:207], v[228:243]
	v_exp_f32_e32 v64, v64
	v_exp_f32_e32 v65, v65
	v_exp_f32_e32 v66, v66
	v_exp_f32_e32 v67, v67
	s_waitcnt vmcnt(3)
	v_mul_u32_u24_sdwa v225, s32, v2 dst_sel:DWORD dst_unused:UNUSED_PAD src0_sel:DWORD src1_sel:BYTE_0
	v_and_b32_e32 v225, -16, v225
	v_mul_u32_u24_sdwa v226, s32, v2 dst_sel:DWORD dst_unused:UNUSED_PAD src0_sel:DWORD src1_sel:BYTE_1
	v_and_b32_e32 v226, -16, v226
	v_mul_u32_u24_sdwa v248, s32, v2 dst_sel:DWORD dst_unused:UNUSED_PAD src0_sel:DWORD src1_sel:BYTE_2
	v_and_b32_e32 v248, -16, v248
	v_mul_u32_u24_sdwa v249, s32, v2 dst_sel:DWORD dst_unused:UNUSED_PAD src0_sel:DWORD src1_sel:BYTE_3
	v_and_b32_e32 v249, -16, v249
	s_waitcnt vmcnt(3) lgkmcnt(0)
	s_barrier
	s_andn2_b64 vcc, exec, s[42:43]
	s_cbranch_vccnz .LBB0_1279
	s_waitcnt lgkmcnt(0)
	ds_read_b128 v[86:89], v85 offset:49248
	ds_read_b128 v[90:93], v85 offset:49216
	ds_read_b128 v[94:97], v85 offset:49184
	ds_read_b128 v[98:101], v85 offset:49152
	s_waitcnt lgkmcnt(3)
	v_pk_mul_f32 v[32:33], v[32:33], v[86:87]
	s_waitcnt lgkmcnt(2)
	v_pk_mul_f32 v[28:29], v[28:29], v[90:91]
	s_waitcnt lgkmcnt(1)
	v_pk_mul_f32 v[24:25], v[24:25], v[94:95]
	v_pk_mul_f32 v[34:35], v[34:35], v[88:89]
	v_pk_mul_f32 v[30:31], v[30:31], v[92:93]
	v_pk_mul_f32 v[26:27], v[26:27], v[96:97]
	s_waitcnt lgkmcnt(0)
	v_pk_mul_f32 v[22:23], v[22:23], v[100:101]
	v_pk_mul_f32 v[20:21], v[20:21], v[98:99]
	v_pk_mul_f32 v[16:17], v[16:17], v[86:87]
	v_pk_mul_f32 v[12:13], v[12:13], v[90:91]
	v_pk_mul_f32 v[8:9], v[8:9], v[94:95]
	v_pk_mul_f32 v[18:19], v[18:19], v[88:89]
	v_pk_mul_f32 v[14:15], v[14:15], v[92:93]
	v_pk_mul_f32 v[10:11], v[10:11], v[96:97]
	v_pk_mul_f32 v[6:7], v[6:7], v[100:101]
	v_pk_mul_f32 v[4:5], v[4:5], v[98:99]
	v_pk_mul_f32 v[240:241], v[240:241], v[86:87]
	v_pk_mul_f32 v[236:237], v[236:237], v[90:91]
	v_pk_mul_f32 v[232:233], v[232:233], v[94:95]
	v_pk_mul_f32 v[242:243], v[242:243], v[88:89]
	v_pk_mul_f32 v[238:239], v[238:239], v[92:93]
	v_pk_mul_f32 v[234:235], v[234:235], v[96:97]
	v_pk_mul_f32 v[230:231], v[230:231], v[100:101]
	v_pk_mul_f32 v[228:229], v[228:229], v[98:99]

; #define WAIT_BAR(N) asm volatile("s_waitcnt vmcnt(" #N ") lgkmcnt(0)\n\ts_barrier":::"memory")
;   #define RESC() do{ if(resc){ asm volatile("s_waitcnt lgkmcnt(0)":::"memory"); \
;       _Pragma("unroll") for(int d_=0;d_<2;++d_) _Pragma("unroll") for(int r=0;r<16;++r)o[d_][r]*=wsf[crow(r,hi)]; } }while(0)
;   #define ROT() do{sl_prev=sl_cur;sl_cur=sl_next;sl_next=(sl_next==(NSLOT-1)*SLOTB)?0:sl_next+SLOTB;}while(0)
;   #define ENDW(tt) do{ if((tt)+3<NT){WAIT_BAR(2);} else if((tt)+2<NT){WAIT_BAR(1);} else {WAIT_BAR(0);} }while(0)
; template<int THRL> __device__ __forceinline__ void attn_unit(int b,int h,int qb,const bf16*Q,const bf16*__restrict__ K,const bf16*__restrict__ V,bf16*O,const unsigned*MASK,char*shm){
;     ...
;   int t=1;
;   for(;t+5<NT;t+=2){
;     STEP(pB0,pB1,pA0,pA1,t,true,true,true,wB,wA);     WAIT_BAR(2); RESC(); ROT();
;     STEP(pA0,pA1,pB0,pB1,t+1,true,true,true,wA,wB);   WAIT_BAR(2); RESC(); ROT();
;   }
;     ...
;   for(;t+1<NT;t+=2){
;     STEP(pB0,pB1,pA0,pA1,t,(t+3<NT),(t+1<NT),(t+1<NT),wB,wA);       ENDW(t);   RESC(); ROT();
;     STEP(pA0,pA1,pB0,pB1,t+1,(t+4<NT),(t+2<NT),(t+2<NT),wA,wB);     ENDW(t+1); RESC(); ROT();
.LBB0_1293:
	s_waitcnt lgkmcnt(0)
	v_and_b32_e32 v146, v146, v80
	v_and_b32_e32 v147, v147, v81
	v_and_b32_e32 v148, v148, v82
	v_and_b32_e32 v149, v149, v83
	ds_read_b128 v[80:83], v226 offset:51200
	s_waitcnt lgkmcnt(14)
	v_mfma_f32_32x32x16_bf16 v[20:35], v[146:149], v[186:189], v[20:35]
	v_exp_f32_e32 v102, v102
	v_exp_f32_e32 v103, v103
	v_exp_f32_e32 v104, v104
	v_exp_f32_e32 v105, v105
	s_waitcnt lgkmcnt(12)
	v_mfma_f32_32x32x16_bf16 v[4:19], v[146:149], v[178:181], v[4:19]
	v_mfma_f32_32x32x16_bf16 v[228:243], v[146:149], v[204:207], v[228:243]
	v_exp_f32_e32 v106, v106
	v_exp_f32_e32 v107, v107
	v_exp_f32_e32 v108, v108
	v_exp_f32_e32 v109, v109
	s_waitcnt lgkmcnt(0)
	v_and_b32_e32 v142, v142, v80
	v_and_b32_e32 v143, v143, v81
	v_and_b32_e32 v144, v144, v82
	v_and_b32_e32 v145, v145, v83
	ds_read_b128 v[80:83], v248 offset:51200
	v_add_u32_e32 v60, s62, v221
	ds_read_b128 v[178:181], v60
	ds_read_b128 v[170:173], v60 offset:512
	s_waitcnt lgkmcnt(12)
	v_mfma_f32_32x32x16_bf16 v[20:35], v[142:145], v[182:185], v[20:35]
	v_exp_f32_e32 v110, v110
	v_exp_f32_e32 v111, v111
	v_exp_f32_e32 v112, v112
	v_exp_f32_e32 v113, v113
	ds_read_b128 v[174:177], v60 offset:2048
	ds_read_b128 v[162:165], v60 offset:2560
	s_waitcnt lgkmcnt(12)
	v_mfma_f32_32x32x16_bf16 v[4:19], v[142:145], v[76:79], v[4:19]
	v_mfma_f32_32x32x16_bf16 v[228:243], v[142:145], v[204:207], v[228:243]
	v_exp_f32_e32 v114, v114
	v_exp_f32_e32 v115, v115
	v_exp_f32_e32 v116, v116
	v_exp_f32_e32 v117, v117
	s_waitcnt lgkmcnt(4)
	v_and_b32_e32 v130, v130, v80
	v_and_b32_e32 v131, v131, v81
	v_and_b32_e32 v132, v132, v82
	v_and_b32_e32 v133, v133, v83
	ds_read_b128 v[80:83], v249 offset:51200
	ds_read_b128 v[166:169], v60 offset:4096
	ds_read_b128 v[154:157], v60 offset:4608
	s_waitcnt lgkmcnt(12)
	v_mfma_f32_32x32x16_bf16 v[20:35], v[130:133], v[72:75], v[20:35]
	v_exp_f32_e32 v86, v86
	v_exp_f32_e32 v87, v87
	v_exp_f32_e32 v88, v88
	v_exp_f32_e32 v89, v89
	ds_read_b128 v[158:161], v60 offset:6144
	ds_read_b128 v[150:153], v60 offset:6656
	s_waitcnt lgkmcnt(12)
	v_mfma_f32_32x32x16_bf16 v[4:19], v[130:133], v[68:71], v[4:19]
	v_mfma_f32_32x32x16_bf16 v[228:243], v[130:133], v[204:207], v[228:243]
	v_exp_f32_e32 v90, v90
	v_exp_f32_e32 v91, v91
	v_exp_f32_e32 v92, v92
	v_exp_f32_e32 v93, v93
	s_waitcnt lgkmcnt(4)
	v_and_b32_e32 v118, v118, v80
	v_and_b32_e32 v119, v119, v81
	v_and_b32_e32 v120, v120, v82
	v_and_b32_e32 v121, v121, v83
	s_nop 0
	s_waitcnt lgkmcnt(10)
	v_mfma_f32_32x32x16_bf16 v[20:35], v[118:121], v[56:59], v[20:35]
	v_exp_f32_e32 v94, v94
	v_exp_f32_e32 v95, v95
	v_exp_f32_e32 v96, v96
	v_exp_f32_e32 v97, v97
	s_waitcnt lgkmcnt(8)
	v_mfma_f32_32x32x16_bf16 v[4:19], v[118:121], v[52:55], v[4:19]
	v_mfma_f32_32x32x16_bf16 v[228:243], v[118:121], v[204:207], v[228:243]
	v_exp_f32_e32 v98, v98
	v_exp_f32_e32 v99, v99
	v_exp_f32_e32 v100, v100
	v_exp_f32_e32 v101, v101
	v_mul_u32_u24_sdwa v225, s32, v218 dst_sel:DWORD dst_unused:UNUSED_PAD src0_sel:DWORD src1_sel:BYTE_0
	v_and_b32_e32 v225, -16, v225
	v_mul_u32_u24_sdwa v226, s32, v218 dst_sel:DWORD dst_unused:UNUSED_PAD src0_sel:DWORD src1_sel:BYTE_1
	v_and_b32_e32 v226, -16, v226
	v_mul_u32_u24_sdwa v248, s32, v218 dst_sel:DWORD dst_unused:UNUSED_PAD src0_sel:DWORD src1_sel:BYTE_2
	v_and_b32_e32 v248, -16, v248
	v_mul_u32_u24_sdwa v249, s32, v218 dst_sel:DWORD dst_unused:UNUSED_PAD src0_sel:DWORD src1_sel:BYTE_3
	v_and_b32_e32 v249, -16, v249
	s_mov_b64 s[4:5], -1
	s_and_b64 vcc, exec, s[48:49]
	s_cbranch_vccnz .LBB0_1318
	s_andn2_b64 vcc, exec, s[4:5]
	s_cbranch_vccz .LBB0_1323

; #define WAIT_BAR(N) asm volatile("s_waitcnt vmcnt(" #N ") lgkmcnt(0)\n\ts_barrier":::"memory")
;   #define RESC() do{ if(resc){ asm volatile("s_waitcnt lgkmcnt(0)":::"memory"); \
;       _Pragma("unroll") for(int d_=0;d_<2;++d_) _Pragma("unroll") for(int r=0;r<16;++r)o[d_][r]*=wsf[crow(r,hi)]; } }while(0)
;   #define ROT() do{sl_prev=sl_cur;sl_cur=sl_next;sl_next=(sl_next==(NSLOT-1)*SLOTB)?0:sl_next+SLOTB;}while(0)
;   #define ENDW(tt) do{ if((tt)+3<NT){WAIT_BAR(2);} else if((tt)+2<NT){WAIT_BAR(1);} else {WAIT_BAR(0);} }while(0)
; template<int THRL> __device__ __forceinline__ void attn_unit(int b,int h,int qb,const bf16*Q,const bf16*__restrict__ K,const bf16*__restrict__ V,bf16*O,const unsigned*MASK,char*shm){
;     ...
;   int t=1;
;   for(;t+5<NT;t+=2){
;     STEP(pB0,pB1,pA0,pA1,t,true,true,true,wB,wA);     WAIT_BAR(2); RESC(); ROT();
;     STEP(pA0,pA1,pB0,pB1,t+1,true,true,true,wA,wB);   WAIT_BAR(2); RESC(); ROT();
;   }
;     ...
;   for(;t+1<NT;t+=2){
;     STEP(pB0,pB1,pA0,pA1,t,(t+3<NT),(t+1<NT),(t+1<NT),wB,wA);       ENDW(t);   RESC(); ROT();
;     STEP(pA0,pA1,pB0,pB1,t+1,(t+4<NT),(t+2<NT),(t+2<NT),wA,wB);     ENDW(t+1); RESC(); ROT();
.LBB0_1312:
	s_waitcnt lgkmcnt(4)
	v_mfma_f32_32x32x16_bf16 v[4:19], v[130:133], v[102:105], v[4:19]
	v_mfma_f32_32x32x16_bf16 v[228:243], v[130:133], v[204:207], v[228:243]
	v_exp_f32_e32 v56, v56
	v_exp_f32_e32 v57, v57
	v_exp_f32_e32 v58, v58
	v_exp_f32_e32 v59, v59
	s_waitcnt lgkmcnt(0)
	v_and_b32_e32 v118, v118, v114
	v_and_b32_e32 v119, v119, v115
	v_and_b32_e32 v120, v120, v116
	v_and_b32_e32 v121, v121, v117
	s_nop 0
	s_waitcnt lgkmcnt(2)
	v_mfma_f32_32x32x16_bf16 v[20:35], v[118:121], v[90:93], v[20:35]
	v_exp_f32_e32 v60, v60
	v_exp_f32_e32 v61, v61
	v_exp_f32_e32 v62, v62
	v_exp_f32_e32 v63, v63
	s_waitcnt lgkmcnt(0)
	v_mfma_f32_32x32x16_bf16 v[4:19], v[118:121], v[86:89], v[4:19]
	v_mfma_f32_32x32x16_bf16 v[228:243], v[118:121], v[204:207], v[228:243]
	v_exp_f32_e32 v64, v64
	v_exp_f32_e32 v65, v65
	v_exp_f32_e32 v66, v66
	v_exp_f32_e32 v67, v67
	v_mul_u32_u24_sdwa v225, s32, v223 dst_sel:DWORD dst_unused:UNUSED_PAD src0_sel:DWORD src1_sel:BYTE_0
	v_and_b32_e32 v225, -16, v225
	v_mul_u32_u24_sdwa v226, s32, v223 dst_sel:DWORD dst_unused:UNUSED_PAD src0_sel:DWORD src1_sel:BYTE_1
	v_and_b32_e32 v226, -16, v226
	v_mul_u32_u24_sdwa v248, s32, v223 dst_sel:DWORD dst_unused:UNUSED_PAD src0_sel:DWORD src1_sel:BYTE_2
	v_and_b32_e32 v248, -16, v248
	v_mul_u32_u24_sdwa v249, s32, v223 dst_sel:DWORD dst_unused:UNUSED_PAD src0_sel:DWORD src1_sel:BYTE_3
	v_and_b32_e32 v249, -16, v249
	s_mov_b64 s[4:5], -1
	s_and_b64 vcc, exec, s[50:51]
	s_cbranch_vccnz .LBB0_1324
	s_andn2_b64 vcc, exec, s[4:5]
	s_cbranch_vccz .LBB0_1329

; #define SBAR() __builtin_amdgcn_sched_barrier(0)
; #define WAIT_BAR(N) asm volatile("s_waitcnt vmcnt(" #N ") lgkmcnt(0)\n\ts_barrier":::"memory")
;   #define RESC() do{ if(resc){ asm volatile("s_waitcnt lgkmcnt(0)":::"memory"); \
;       _Pragma("unroll") for(int d_=0;d_<2;++d_) _Pragma("unroll") for(int r=0;r<16;++r)o[d_][r]*=wsf[crow(r,hi)]; } }while(0)
;   #define ROT() do{sl_prev=sl_cur;sl_cur=sl_next;sl_next=(sl_next==(NSLOT-1)*SLOTB)?0:sl_next+SLOTB;}while(0)
;   #define PKW(P,B) cvtpk_s(P[B],P[B+1])
;   #define ENDW(tt) do{ if((tt)+3<NT){WAIT_BAR(2);} else if((tt)+2<NT){WAIT_BAR(1);} else {WAIT_BAR(0);} }while(0)
; template<int THRL> __device__ __forceinline__ void attn_unit(int b,int h,int qb,const bf16*Q,const bf16*__restrict__ K,const bf16*__restrict__ V,bf16*O,const unsigned*MASK,char*shm){
;     ...
;   int t=1;
;   for(;t+5<NT;t+=2){
;     STEP(pB0,pB1,pA0,pA1,t,true,true,true,wB,wA);     WAIT_BAR(2); RESC(); ROT();
;     STEP(pA0,pA1,pB0,pB1,t+1,true,true,true,wA,wB);   WAIT_BAR(2); RESC(); ROT();
;   }
;     ...
;   for(;t+1<NT;t+=2){
;     STEP(pB0,pB1,pA0,pA1,t,(t+3<NT),(t+1<NT),(t+1<NT),wB,wA);       ENDW(t);   RESC(); ROT();
;     STEP(pA0,pA1,pB0,pB1,t+1,(t+4<NT),(t+2<NT),(t+2<NT),wA,wB);     ENDW(t+1); RESC(); ROT();
;   }
;   STEP(pB0,pB1,pA0,pA1,NT-1,false,false,false,wB,wA); RESC();
;   { float sacc=pB0[0]+pB0[1]; _Pragma("unroll") for(int r=2;r<16;++r)sacc+=pB0[r]; _Pragma("unroll") for(int r=0;r<16;++r)sacc+=pB1[r]; l_reg+=sacc;
;     pw0=(u32x4){PKW(pB0,0),PKW(pB0,2),PKW(pB0,4),PKW(pB0,6)};pw1=(u32x4){PKW(pB0,8),PKW(pB0,10),PKW(pB0,12),PKW(pB0,14)};pw2=(u32x4){PKW(pB1,0),PKW(pB1,2),PKW(pB1,4),PKW(pB1,6)};pw3=(u32x4){PKW(pB1,8),PKW(pB1,10),PKW(pB1,12),PKW(pB1,14)};
;     SBAR(); pv(o,vb0+sl_cur,PAF(0),PAF(1),PAF(2),PAF(3)); }
.LBB0_1338:
	s_waitcnt lgkmcnt(0)
	v_and_b32_e32 v146, v146, v154
	v_and_b32_e32 v147, v147, v155
	v_and_b32_e32 v148, v148, v156
	v_and_b32_e32 v149, v149, v157
	ds_read_b128 v[154:157], v226 offset:51200
	s_waitcnt lgkmcnt(14)
	v_mfma_f32_32x32x16_bf16 v[20:35], v[146:149], v[114:117], v[20:35]
	v_exp_f32_e32 v86, v86
	v_exp_f32_e32 v87, v87
	v_exp_f32_e32 v88, v88
	v_exp_f32_e32 v89, v89
	s_waitcnt lgkmcnt(12)
	v_mfma_f32_32x32x16_bf16 v[4:19], v[146:149], v[110:113], v[4:19]
	v_mfma_f32_32x32x16_bf16 v[228:243], v[146:149], v[204:207], v[228:243]
	v_exp_f32_e32 v90, v90
	v_exp_f32_e32 v91, v91
	v_exp_f32_e32 v92, v92
	v_exp_f32_e32 v93, v93
	s_waitcnt lgkmcnt(0)
	v_and_b32_e32 v142, v142, v154
	v_and_b32_e32 v143, v143, v155
	v_and_b32_e32 v144, v144, v156
	v_and_b32_e32 v145, v145, v157
	ds_read_b128 v[154:157], v248 offset:51200
	s_waitcnt lgkmcnt(10)
	v_mfma_f32_32x32x16_bf16 v[20:35], v[142:145], v[106:109], v[20:35]
	v_exp_f32_e32 v94, v94
	v_exp_f32_e32 v95, v95
	v_exp_f32_e32 v96, v96
	v_exp_f32_e32 v97, v97
	s_waitcnt lgkmcnt(8)
	v_mfma_f32_32x32x16_bf16 v[4:19], v[142:145], v[102:105], v[4:19]
	v_mfma_f32_32x32x16_bf16 v[228:243], v[142:145], v[204:207], v[228:243]
	v_exp_f32_e32 v98, v98
	v_exp_f32_e32 v99, v99
	v_exp_f32_e32 v100, v100
	v_exp_f32_e32 v101, v101
	s_waitcnt lgkmcnt(0)
	v_and_b32_e32 v130, v130, v154
	v_and_b32_e32 v131, v131, v155
	v_and_b32_e32 v132, v132, v156
	v_and_b32_e32 v133, v133, v157
	ds_read_b128 v[154:157], v249 offset:51200
	s_waitcnt lgkmcnt(6)
	v_mfma_f32_32x32x16_bf16 v[20:35], v[130:133], v[80:83], v[20:35]
	v_exp_f32_e32 v36, v36
	v_exp_f32_e32 v37, v37
	v_exp_f32_e32 v38, v38
	v_exp_f32_e32 v39, v39
	s_waitcnt lgkmcnt(4)
	v_mfma_f32_32x32x16_bf16 v[4:19], v[130:133], v[76:79], v[4:19]
	v_mfma_f32_32x32x16_bf16 v[228:243], v[130:133], v[204:207], v[228:243]
	v_exp_f32_e32 v40, v40
	v_exp_f32_e32 v41, v41
	v_exp_f32_e32 v42, v42
	v_exp_f32_e32 v43, v43
	s_waitcnt lgkmcnt(0)
	v_and_b32_e32 v118, v118, v154
	v_and_b32_e32 v119, v119, v155
	v_and_b32_e32 v120, v120, v156
	v_and_b32_e32 v121, v121, v157
	s_nop 0
	s_waitcnt lgkmcnt(2)
	v_mfma_f32_32x32x16_bf16 v[20:35], v[118:121], v[72:75], v[20:35]
	v_exp_f32_e32 v44, v44
	v_exp_f32_e32 v45, v45
	v_exp_f32_e32 v46, v46
	v_exp_f32_e32 v47, v47
	s_waitcnt lgkmcnt(0)
	v_mfma_f32_32x32x16_bf16 v[4:19], v[118:121], v[68:71], v[4:19]
	v_mfma_f32_32x32x16_bf16 v[228:243], v[118:121], v[204:207], v[228:243]
	v_exp_f32_e32 v48, v48
	v_exp_f32_e32 v49, v49
	v_exp_f32_e32 v50, v50
	v_exp_f32_e32 v51, v51
	v_mul_u32_u24_sdwa v225, s32, v218 dst_sel:DWORD dst_unused:UNUSED_PAD src0_sel:DWORD src1_sel:BYTE_0
	v_and_b32_e32 v225, -16, v225
	v_mul_u32_u24_sdwa v226, s32, v218 dst_sel:DWORD dst_unused:UNUSED_PAD src0_sel:DWORD src1_sel:BYTE_1
	v_and_b32_e32 v226, -16, v226
	v_mul_u32_u24_sdwa v248, s32, v218 dst_sel:DWORD dst_unused:UNUSED_PAD src0_sel:DWORD src1_sel:BYTE_2
	v_and_b32_e32 v248, -16, v248
	v_mul_u32_u24_sdwa v249, s32, v218 dst_sel:DWORD dst_unused:UNUSED_PAD src0_sel:DWORD src1_sel:BYTE_3
	v_and_b32_e32 v249, -16, v249
	s_andn2_b64 vcc, exec, s[40:41]
	v_lshl_add_u32 v52, v214, 4, s57
	s_cbranch_vccnz .LBB0_1340
	s_waitcnt lgkmcnt(0)
	ds_read_b128 v[54:57], v52 offset:49248
	ds_read_b128 v[58:61], v52 offset:49216
	ds_read_b128 v[62:65], v52 offset:49184
	ds_read_b128 v[66:69], v52 offset:49152
	s_waitcnt lgkmcnt(3)
	v_pk_mul_f32 v[34:35], v[34:35], v[56:57]
	s_waitcnt lgkmcnt(2)
	v_pk_mul_f32 v[30:31], v[30:31], v[60:61]
	s_waitcnt lgkmcnt(1)
	v_pk_mul_f32 v[26:27], v[26:27], v[64:65]
	s_waitcnt lgkmcnt(0)
	v_pk_mul_f32 v[22:23], v[22:23], v[68:69]
	v_pk_mul_f32 v[32:33], v[32:33], v[54:55]
	v_pk_mul_f32 v[28:29], v[28:29], v[58:59]
	v_pk_mul_f32 v[24:25], v[24:25], v[62:63]
	v_pk_mul_f32 v[20:21], v[20:21], v[66:67]
	v_pk_mul_f32 v[18:19], v[18:19], v[56:57]
	v_pk_mul_f32 v[14:15], v[14:15], v[60:61]
	v_pk_mul_f32 v[10:11], v[10:11], v[64:65]
	v_pk_mul_f32 v[6:7], v[6:7], v[68:69]
	v_pk_mul_f32 v[16:17], v[16:17], v[54:55]
	v_pk_mul_f32 v[12:13], v[12:13], v[58:59]
	v_pk_mul_f32 v[8:9], v[8:9], v[62:63]
	v_pk_mul_f32 v[4:5], v[4:5], v[66:67]
	v_pk_mul_f32 v[242:243], v[242:243], v[56:57]
	v_pk_mul_f32 v[238:239], v[238:239], v[60:61]
	v_pk_mul_f32 v[234:235], v[234:235], v[64:65]
	v_pk_mul_f32 v[230:231], v[230:231], v[68:69]
	v_pk_mul_f32 v[240:241], v[240:241], v[54:55]
	v_pk_mul_f32 v[236:237], v[236:237], v[58:59]
	v_pk_mul_f32 v[232:233], v[232:233], v[62:63]
	v_pk_mul_f32 v[228:229], v[228:229], v[66:67]
